# v50: window/SWA sub-tile1 K-frag LDS reads hoisted into sub-tile0 after QK; ring DMA issue block moved into sub-tile0 LDS-latency window
# baseline (speedup 1.0000x reference)
.LBB0_510:
	s_waitcnt lgkmcnt(0)
	s_add_i32 s21, s21, -1
	s_add_i32 s2, s26, s21
	s_addk_i32 s30, 0x4000
	s_add_i32 s25, s25, 1
	s_sub_i32 s22, s22, 64
	s_add_i32 s19, s19, 64
	s_cmp_eq_u32 s2, 0
	s_cbranch_scc1 .LBB0_533

.Lw_win_4_done:
.LBB0_519:
	s_cmp_eq_u32 s32, 0
	s_cselect_b32 s84, 0, 1
	s_sub_u32 s32, s32, s84
	s_add_i32 s2, s29, s22
	s_add_i32 s3, s27, s21
	s_add_i32 s3, s3, -1
	s_and_b32 s31, s30, 0xc000
	s_add_i32 s33, s31, 0
	s_ashr_i32 s3, s3, 2
	s_add_i32 s31, s2, 0x7e0
	s_cmp_gt_i32 s31, s23
	v_cvt_f32_i32_e32 v111, s3
	s_cselect_b64 s[34:35], -1, 0
	s_add_i32 s3, s2, 0x7ff
	s_cmp_lt_i32 s3, s24
	s_cselect_b64 s[38:39], -1, 0
	v_add_u32_e32 v2, s33, v101
	v_add_u32_e32 v4, s33, v102
	v_add_u32_e32 v5, s33, v103
	v_add_u32_e32 v6, s33, v104
	s_or_b64 s[34:35], s[34:35], s[38:39]
	s_and_b64 vcc, exec, s[34:35]
	v_add_u32_e32 v115, v2, v100
	v_add_u32_e32 v114, v4, v100
	v_add_u32_e32 v113, v5, v100
	v_add_u32_e32 v112, v6, v100
	v_add_u32_e32 v16, s33, v105
	v_add_u32_e32 v17, s33, v106
	s_barrier
	ds_read_b128 v[4:7], v115 offset:4096
	ds_read_b128 v[188:191], v114 offset:4096
	ds_read_b128 v[192:195], v113 offset:4096
	ds_read_b128 v[202:205], v112 offset:4096
	s_cmp_gt_i32 s25, s17
	s_cbranch_scc1 .Lring_issue_skip_0
	s_add_i32 s85, s2, 0x700
	s_mul_hi_i32 s86, s85, 0x3600
	s_mulk_i32 s85, 0x3600
	s_add_u32 s88, s12, s85
	s_addc_u32 s89, s13, s86
	s_add_u32 s90, s14, s85
	s_addc_u32 s91, s15, s86
	s_add_i32 s85, s30, 0xc000
	s_and_b32 s85, s85, 0xc000
	v_add_u32_e32 v151, s85, v97
	v_mov_b32_e32 v150, v95
	v_readfirstlane_b32 s85, v151
	v_add_u32_e32 v151, 0x2000, v151
	s_mov_b32 m0, s85
	v_readfirstlane_b32 s85, v151
	global_load_lds_dwordx4 v150, s[88:89]
	v_mov_b32_e32 v150, v96
	s_mov_b32 m0, s85
	s_nop 0
	global_load_lds_dwordx4 v150, s[90:91]
.Lring_issue_skip_0:
	s_cbranch_vccnz .Lkpre_skip_w
	s_and_b32 s31, s31, 0xe0
	v_or_b32_e32 v2, s31, v99
	v_cvt_f32_ubyte0_e32 v2, v2
	v_and_b32_e32 v2, 0x7fff0000, v2
	v_or_b32_sdwa v2, v2, v111 dst_sel:DWORD dst_unused:UNUSED_PAD src0_sel:DWORD src1_sel:WORD_1
	v_cndmask_b32_e64 v246, 0, v2, s[36:37]
	s_cmp_ge_i32 s20, s3
	s_cselect_b64 s[34:35], -1, 0
	s_waitcnt lgkmcnt(3)
	s_setprio 1
	v_mfma_f32_32x32x16_bf16 v[50:65], v[4:7], v[74:77], 0
	s_sub_i32 s3, s19, 32
	s_cmpk_lt_i32 s3, 0x1e1
	v_add3_u32 v116, v17, v94, s69
	s_cselect_b64 s[38:39], -1, 0
	s_and_b64 s[34:35], s[34:35], s[38:39]
	s_and_b64 vcc, exec, s[34:35]
	s_waitcnt lgkmcnt(2)
	v_mfma_f32_32x32x16_bf16 v[50:65], v[188:191], v[66:69], v[50:65]
	s_waitcnt lgkmcnt(1)
	v_mfma_f32_32x32x16_bf16 v[50:65], v[192:195], v[70:73], v[50:65]
	s_waitcnt lgkmcnt(0)
	v_mfma_f32_32x32x16_bf16 v[50:65], v[202:205], v[78:81], v[50:65]
	v_mfma_f32_32x32x16_bf16 v[50:65], v[246:249], v[82:85], v[50:65]
	v_add3_u32 v2, v16, v94, s69
	ds_read_b64_tr_b16 v[86:87], v2
	ds_read_b64_tr_b16 v[88:89], v2 offset:1024
	ds_read_b64_tr_b16 v[12:13], v116
	ds_read_b64_tr_b16 v[14:15], v116 offset:1024
	ds_read_b64_tr_b16 v[8:9], v2 offset:2048
	ds_read_b64_tr_b16 v[10:11], v2 offset:3072
	ds_read_b64_tr_b16 v[4:5], v116 offset:2048
	ds_read_b64_tr_b16 v[6:7], v116 offset:3072
	ds_read_b128 v[188:191], v115
	ds_read_b128 v[192:195], v114
	ds_read_b128 v[202:205], v113
	s_cbranch_vccnz .LBB0_524
	v_add_u32_e32 v2, s19, v108
	v_subrev_u32_e32 v116, 32, v2
	v_cmp_gt_u32_e32 vcc, s79, v116
	v_add3_u32 v116, v109, s22, 32
	s_nop 5
	v_cndmask_b32_e32 v50, v197, v50, vcc
	v_cmp_lt_u32_e32 vcc, s80, v116
	v_subrev_u32_e32 v116, 34, v2
	s_nop 0
	v_cndmask_b32_e32 v51, v197, v51, vcc
	v_cmp_gt_u32_e32 vcc, s79, v116
	v_subrev_u32_e32 v116, 35, v2
	s_nop 0
	v_cndmask_b32_e32 v52, v197, v52, vcc
	v_cmp_gt_u32_e32 vcc, s79, v116
	v_subrev_u32_e32 v116, 40, v2
	s_nop 0
	v_cndmask_b32_e32 v53, v197, v53, vcc
	v_cmp_gt_u32_e32 vcc, s79, v116
	v_subrev_u32_e32 v116, 41, v2
	s_nop 0
	v_cndmask_b32_e32 v54, v197, v54, vcc
	v_cmp_gt_u32_e32 vcc, s79, v116
	v_subrev_u32_e32 v116, 42, v2
	s_nop 0
	v_cndmask_b32_e32 v55, v197, v55, vcc
	v_cmp_gt_u32_e32 vcc, s79, v116
	v_subrev_u32_e32 v116, 43, v2
	s_nop 0
	v_cndmask_b32_e32 v56, v197, v56, vcc
	v_cmp_gt_u32_e32 vcc, s79, v116
	v_subrev_u32_e32 v116, 48, v2
	s_nop 0
	v_cndmask_b32_e32 v57, v197, v57, vcc
	v_cmp_gt_u32_e32 vcc, s79, v116
	v_subrev_u32_e32 v116, 49, v2
	s_nop 0
	v_cndmask_b32_e32 v58, v197, v58, vcc
	v_cmp_gt_u32_e32 vcc, s79, v116
	v_subrev_u32_e32 v116, 50, v2
	s_nop 0
	v_cndmask_b32_e32 v59, v197, v59, vcc
	v_cmp_gt_u32_e32 vcc, s79, v116
	v_subrev_u32_e32 v116, 51, v2
	s_nop 0
	v_cndmask_b32_e32 v60, v197, v60, vcc
	v_cmp_gt_u32_e32 vcc, s79, v116
	v_subrev_u32_e32 v116, 56, v2
	s_nop 0
	v_cndmask_b32_e32 v61, v197, v61, vcc
	v_cmp_gt_u32_e32 vcc, s79, v116
	v_subrev_u32_e32 v116, 57, v2
	s_nop 0
	v_cndmask_b32_e32 v62, v197, v62, vcc
	v_cmp_gt_u32_e32 vcc, s79, v116
	v_subrev_u32_e32 v116, 58, v2
	v_subrev_u32_e32 v2, 59, v2
	v_cndmask_b32_e32 v63, v197, v63, vcc
	v_cmp_gt_u32_e32 vcc, s79, v116
	s_nop 1
	v_cndmask_b32_e32 v64, v197, v64, vcc
	v_cmp_gt_u32_e32 vcc, s79, v2
	s_nop 1
	v_cndmask_b32_e32 v65, v197, v65, vcc

.LBB0_527:
	s_add_i32 s3, s2, 0x7c0
	s_cmp_gt_i32 s3, s23
	s_cselect_b64 s[34:35], -1, 0
	s_addk_i32 s2, 0x7df
	s_cmp_lt_i32 s2, s24
	s_cselect_b64 s[38:39], -1, 0
	s_or_b64 s[34:35], s[34:35], s[38:39]
	s_and_b64 vcc, exec, s[34:35]
	s_cbranch_vccnz .LBB0_510
	ds_read_b128 v[4:7], v112
	s_and_b32 s3, s3, 0xc0
	v_or_b32_e32 v2, s3, v99
	v_cvt_f32_ubyte0_e32 v2, v2
	v_and_b32_e32 v2, 0x7fff0000, v2
	v_or_b32_sdwa v2, v2, v111 dst_sel:DWORD dst_unused:UNUSED_PAD src0_sel:DWORD src1_sel:WORD_1
	v_cndmask_b32_e64 v246, 0, v2, s[36:37]
	s_cmp_ge_i32 s20, s2
	s_cselect_b64 s[2:3], -1, 0
	s_waitcnt lgkmcnt(1)
	s_setprio 1
	v_mfma_f32_32x32x16_bf16 v[50:65], v[188:191], v[74:77], 0
	s_cmpk_lt_i32 s19, 0x1e1
	s_cselect_b64 s[34:35], -1, 0
	s_and_b64 s[2:3], s[2:3], s[34:35]
	s_and_b64 vcc, exec, s[2:3]
	v_mfma_f32_32x32x16_bf16 v[50:65], v[192:195], v[66:69], v[50:65]
	v_mfma_f32_32x32x16_bf16 v[50:65], v[202:205], v[70:73], v[50:65]
	s_waitcnt lgkmcnt(0)
	v_mfma_f32_32x32x16_bf16 v[50:65], v[4:7], v[78:81], v[50:65]
	v_mfma_f32_32x32x16_bf16 v[50:65], v[246:249], v[82:85], v[50:65]
	v_add3_u32 v2, v16, v94, s67
	v_add3_u32 v16, v17, v94, s67
	ds_read_b64_tr_b16 v[86:87], v2
	ds_read_b64_tr_b16 v[88:89], v2 offset:1024
	ds_read_b64_tr_b16 v[12:13], v16
	ds_read_b64_tr_b16 v[14:15], v16 offset:1024
	ds_read_b64_tr_b16 v[8:9], v2 offset:2048
	ds_read_b64_tr_b16 v[10:11], v2 offset:3072
	ds_read_b64_tr_b16 v[4:5], v16 offset:2048
	ds_read_b64_tr_b16 v[6:7], v16 offset:3072
	s_cbranch_vccnz .LBB0_530
	v_add_u32_e32 v2, s19, v108
	v_cmp_gt_u32_e32 vcc, s79, v2
	v_add_u32_e32 v16, s22, v109
	s_nop 5
	v_cndmask_b32_e32 v50, v197, v50, vcc
	v_cmp_lt_u32_e32 vcc, s80, v16
	v_add_u32_e32 v16, -2, v2
	s_nop 0
	v_cndmask_b32_e32 v51, v197, v51, vcc
	v_cmp_gt_u32_e32 vcc, s79, v16
	v_add_u32_e32 v16, -3, v2
	s_nop 0
	v_cndmask_b32_e32 v52, v197, v52, vcc
	v_cmp_gt_u32_e32 vcc, s79, v16
	v_add_u32_e32 v16, -8, v2
	s_nop 0
	v_cndmask_b32_e32 v53, v197, v53, vcc
	v_cmp_gt_u32_e32 vcc, s79, v16
	v_add_u32_e32 v16, -9, v2
	s_nop 0
	v_cndmask_b32_e32 v54, v197, v54, vcc
	v_cmp_gt_u32_e32 vcc, s79, v16
	v_add_u32_e32 v16, -10, v2
	s_nop 0
	v_cndmask_b32_e32 v55, v197, v55, vcc
	v_cmp_gt_u32_e32 vcc, s79, v16
	v_add_u32_e32 v16, -11, v2
	s_nop 0
	v_cndmask_b32_e32 v56, v197, v56, vcc
	v_cmp_gt_u32_e32 vcc, s79, v16
	v_add_u32_e32 v16, -16, v2
	s_nop 0
	v_cndmask_b32_e32 v57, v197, v57, vcc
	v_cmp_gt_u32_e32 vcc, s79, v16
	v_subrev_u32_e32 v16, 17, v2
	s_nop 0
	v_cndmask_b32_e32 v58, v197, v58, vcc
	v_cmp_gt_u32_e32 vcc, s79, v16
	v_subrev_u32_e32 v16, 18, v2
	s_nop 0
	v_cndmask_b32_e32 v59, v197, v59, vcc
	v_cmp_gt_u32_e32 vcc, s79, v16
	v_subrev_u32_e32 v16, 19, v2
	s_nop 0
	v_cndmask_b32_e32 v60, v197, v60, vcc
	v_cmp_gt_u32_e32 vcc, s79, v16
	v_subrev_u32_e32 v16, 24, v2
	s_nop 0
	v_cndmask_b32_e32 v61, v197, v61, vcc
	v_cmp_gt_u32_e32 vcc, s79, v16
	v_subrev_u32_e32 v16, 25, v2
	s_nop 0
	v_cndmask_b32_e32 v62, v197, v62, vcc
	v_cmp_gt_u32_e32 vcc, s79, v16
	v_subrev_u32_e32 v16, 26, v2
	v_subrev_u32_e32 v2, 27, v2
	v_cndmask_b32_e32 v63, v197, v63, vcc
	v_cmp_gt_u32_e32 vcc, s79, v16
	s_nop 1
	v_cndmask_b32_e32 v64, v197, v64, vcc
	v_cmp_gt_u32_e32 vcc, s79, v2
	s_nop 1
	v_cndmask_b32_e32 v65, v197, v65, vcc

.Lkpre_skip_w:
	ds_read_b128 v[188:191], v115
	ds_read_b128 v[192:195], v114
	ds_read_b128 v[202:205], v113
	s_branch .LBB0_527

.LBB0_771:
	s_waitcnt lgkmcnt(0)
	s_add_i32 s18, s18, -1
	s_add_i32 s0, s22, s18
	s_addk_i32 s26, 0x4000
	s_add_i32 s21, s21, 1
	s_sub_i32 s17, s17, 64
	s_add_i32 s15, s15, 64
	s_cmp_eq_u32 s0, 0
	s_cbranch_scc1 .LBB0_794

.Lw_swa_4_done:
.LBB0_780:
	s_cmp_eq_u32 s32, 0
	s_cselect_b32 s84, 0, 1
	s_sub_u32 s32, s32, s84
	s_add_i32 s0, s25, s17
	s_add_i32 s1, s23, s18
	s_add_i32 s1, s1, -1
	s_and_b32 s27, s26, 0xc000
	s_add_i32 s34, s27, 0
	s_ashr_i32 s1, s1, 2
	s_add_i32 s27, s0, 0x7e0
	s_cmp_gt_i32 s27, s19
	v_cvt_f32_i32_e32 v114, s1
	s_cselect_b64 s[28:29], -1, 0
	s_add_i32 s1, s0, 0x7ff
	s_cmp_lt_i32 s1, s20
	s_cselect_b64 s[30:31], -1, 0
	v_add_u32_e32 v2, s34, v104
	v_add_u32_e32 v4, s34, v105
	v_add_u32_e32 v5, s34, v106
	v_add_u32_e32 v6, s34, v107
	s_or_b64 s[28:29], s[28:29], s[30:31]
	s_and_b64 vcc, exec, s[28:29]
	v_add_u32_e32 v118, v2, v103
	v_add_u32_e32 v117, v4, v103
	v_add_u32_e32 v116, v5, v103
	v_add_u32_e32 v115, v6, v103
	v_add_u32_e32 v16, s34, v109
	v_add_u32_e32 v17, s34, v110
	s_barrier
	ds_read_b128 v[4:7], v118 offset:4096
	ds_read_b128 v[188:191], v117 offset:4096
	ds_read_b128 v[192:195], v116 offset:4096
	ds_read_b128 v[202:205], v115 offset:4096
	s_cmp_gt_i32 s21, s13
	s_cbranch_scc1 .Lring_issue_skip_1
	s_add_i32 s85, s0, 0x700
	s_mul_hi_i32 s86, s85, 0x3600
	s_mulk_i32 s85, 0x3600
	s_add_u32 s88, s2, s85
	s_addc_u32 s89, s3, s86
	s_add_u32 s90, s10, s85
	s_addc_u32 s91, s11, s86
	s_add_i32 s85, s26, 0xc000
	s_and_b32 s85, s85, 0xc000
	v_add_u32_e32 v151, s85, v99
	v_mov_b32_e32 v150, v97
	v_readfirstlane_b32 s85, v151
	v_add_u32_e32 v151, 0x2000, v151
	s_mov_b32 m0, s85
	v_readfirstlane_b32 s85, v151
	global_load_lds_dwordx4 v150, s[88:89]
	v_mov_b32_e32 v150, v98
	s_mov_b32 m0, s85
	s_nop 0
	global_load_lds_dwordx4 v150, s[90:91]
.Lring_issue_skip_1:
	s_cbranch_vccnz .Lkpre_skip_s
	s_and_b32 s27, s27, 0xe0
	v_or_b32_e32 v2, s27, v102
	v_cvt_f32_ubyte0_e32 v2, v2
	v_and_b32_e32 v2, 0x7fff0000, v2
	v_or_b32_sdwa v2, v2, v114 dst_sel:DWORD dst_unused:UNUSED_PAD src0_sel:DWORD src1_sel:WORD_1
	v_cndmask_b32_e64 v246, 0, v2, s[36:37]
	s_cmp_ge_i32 s16, s1
	s_cselect_b64 s[28:29], -1, 0
	s_waitcnt lgkmcnt(3)
	s_setprio 1
	v_mfma_f32_32x32x16_bf16 v[50:65], v[4:7], v[66:69], 0
	s_sub_i32 s1, s15, 32
	s_cmpk_lt_i32 s1, 0x61
	v_add3_u32 v119, v17, v96, s69
	s_cselect_b64 s[30:31], -1, 0
	s_and_b64 s[28:29], s[28:29], s[30:31]
	s_and_b64 vcc, exec, s[28:29]
	s_waitcnt lgkmcnt(2)
	v_mfma_f32_32x32x16_bf16 v[50:65], v[188:191], v[70:73], v[50:65]
	s_waitcnt lgkmcnt(1)
	v_mfma_f32_32x32x16_bf16 v[50:65], v[192:195], v[74:77], v[50:65]
	s_waitcnt lgkmcnt(0)
	v_mfma_f32_32x32x16_bf16 v[50:65], v[202:205], v[78:81], v[50:65]
	v_mfma_f32_32x32x16_bf16 v[50:65], v[246:249], v[82:85], v[50:65]
	v_add3_u32 v2, v16, v96, s69
	ds_read_b64_tr_b16 v[86:87], v2
	ds_read_b64_tr_b16 v[88:89], v2 offset:1024
	ds_read_b64_tr_b16 v[12:13], v119
	ds_read_b64_tr_b16 v[14:15], v119 offset:1024
	ds_read_b64_tr_b16 v[8:9], v2 offset:2048
	ds_read_b64_tr_b16 v[10:11], v2 offset:3072
	ds_read_b64_tr_b16 v[4:5], v119 offset:2048
	ds_read_b64_tr_b16 v[6:7], v119 offset:3072
	ds_read_b128 v[188:191], v118
	ds_read_b128 v[192:195], v117
	ds_read_b128 v[202:205], v116
	s_cbranch_vccnz .LBB0_785
	v_add_u32_e32 v2, s15, v111
	v_subrev_u32_e32 v119, 32, v2
	v_cmp_gt_u32_e32 vcc, s71, v119
	v_add3_u32 v119, v112, s17, 32
	s_nop 5
	v_cndmask_b32_e32 v50, v197, v50, vcc
	v_cmp_lt_u32_e32 vcc, s47, v119
	v_subrev_u32_e32 v119, 34, v2
	s_nop 0
	v_cndmask_b32_e32 v51, v197, v51, vcc
	v_cmp_gt_u32_e32 vcc, s71, v119
	v_subrev_u32_e32 v119, 35, v2
	s_nop 0
	v_cndmask_b32_e32 v52, v197, v52, vcc
	v_cmp_gt_u32_e32 vcc, s71, v119
	v_subrev_u32_e32 v119, 40, v2
	s_nop 0
	v_cndmask_b32_e32 v53, v197, v53, vcc
	v_cmp_gt_u32_e32 vcc, s71, v119
	v_subrev_u32_e32 v119, 41, v2
	s_nop 0
	v_cndmask_b32_e32 v54, v197, v54, vcc
	v_cmp_gt_u32_e32 vcc, s71, v119
	v_subrev_u32_e32 v119, 42, v2
	s_nop 0
	v_cndmask_b32_e32 v55, v197, v55, vcc
	v_cmp_gt_u32_e32 vcc, s71, v119
	v_subrev_u32_e32 v119, 43, v2
	s_nop 0
	v_cndmask_b32_e32 v56, v197, v56, vcc
	v_cmp_gt_u32_e32 vcc, s71, v119
	v_subrev_u32_e32 v119, 48, v2
	s_nop 0
	v_cndmask_b32_e32 v57, v197, v57, vcc
	v_cmp_gt_u32_e32 vcc, s71, v119
	v_subrev_u32_e32 v119, 49, v2
	s_nop 0
	v_cndmask_b32_e32 v58, v197, v58, vcc
	v_cmp_gt_u32_e32 vcc, s71, v119
	v_subrev_u32_e32 v119, 50, v2
	s_nop 0
	v_cndmask_b32_e32 v59, v197, v59, vcc
	v_cmp_gt_u32_e32 vcc, s71, v119
	v_subrev_u32_e32 v119, 51, v2
	s_nop 0
	v_cndmask_b32_e32 v60, v197, v60, vcc
	v_cmp_gt_u32_e32 vcc, s71, v119
	v_subrev_u32_e32 v119, 56, v2
	s_nop 0
	v_cndmask_b32_e32 v61, v197, v61, vcc
	v_cmp_gt_u32_e32 vcc, s71, v119
	v_subrev_u32_e32 v119, 57, v2
	s_nop 0
	v_cndmask_b32_e32 v62, v197, v62, vcc
	v_cmp_gt_u32_e32 vcc, s71, v119
	v_subrev_u32_e32 v119, 58, v2
	v_subrev_u32_e32 v2, 59, v2
	v_cndmask_b32_e32 v63, v197, v63, vcc
	v_cmp_gt_u32_e32 vcc, s71, v119
	s_nop 1
	v_cndmask_b32_e32 v64, v197, v64, vcc
	v_cmp_gt_u32_e32 vcc, s71, v2
	s_nop 1
	v_cndmask_b32_e32 v65, v197, v65, vcc

.LBB0_788:
	s_add_i32 s1, s0, 0x7c0
	s_cmp_gt_i32 s1, s19
	s_cselect_b64 s[28:29], -1, 0
	s_addk_i32 s0, 0x7df
	s_cmp_lt_i32 s0, s20
	s_cselect_b64 s[30:31], -1, 0
	s_or_b64 s[28:29], s[28:29], s[30:31]
	s_and_b64 vcc, exec, s[28:29]
	s_cbranch_vccnz .LBB0_771
	ds_read_b128 v[4:7], v115
	s_and_b32 s1, s1, 0xc0
	v_or_b32_e32 v2, s1, v102
	v_cvt_f32_ubyte0_e32 v2, v2
	v_and_b32_e32 v2, 0x7fff0000, v2
	v_or_b32_sdwa v2, v2, v114 dst_sel:DWORD dst_unused:UNUSED_PAD src0_sel:DWORD src1_sel:WORD_1
	v_cndmask_b32_e64 v246, 0, v2, s[36:37]
	s_cmp_ge_i32 s16, s0
	s_cselect_b64 s[0:1], -1, 0
	s_waitcnt lgkmcnt(1)
	s_setprio 1
	v_mfma_f32_32x32x16_bf16 v[50:65], v[188:191], v[66:69], 0
	s_cmpk_lt_i32 s15, 0x61
	s_cselect_b64 s[28:29], -1, 0
	s_and_b64 s[0:1], s[0:1], s[28:29]
	s_and_b64 vcc, exec, s[0:1]
	v_mfma_f32_32x32x16_bf16 v[50:65], v[192:195], v[70:73], v[50:65]
	v_mfma_f32_32x32x16_bf16 v[50:65], v[202:205], v[74:77], v[50:65]
	s_waitcnt lgkmcnt(0)
	v_mfma_f32_32x32x16_bf16 v[50:65], v[4:7], v[78:81], v[50:65]
	v_mfma_f32_32x32x16_bf16 v[50:65], v[246:249], v[82:85], v[50:65]
	v_add3_u32 v2, v16, v96, s67
	v_add3_u32 v16, v17, v96, s67
	ds_read_b64_tr_b16 v[86:87], v2
	ds_read_b64_tr_b16 v[88:89], v2 offset:1024
	ds_read_b64_tr_b16 v[12:13], v16
	ds_read_b64_tr_b16 v[14:15], v16 offset:1024
	ds_read_b64_tr_b16 v[8:9], v2 offset:2048
	ds_read_b64_tr_b16 v[10:11], v2 offset:3072
	ds_read_b64_tr_b16 v[4:5], v16 offset:2048
	ds_read_b64_tr_b16 v[6:7], v16 offset:3072
	s_cbranch_vccnz .LBB0_791
	v_add_u32_e32 v2, s15, v111
	v_cmp_gt_u32_e32 vcc, s71, v2
	v_add_u32_e32 v16, s17, v112
	s_nop 5
	v_cndmask_b32_e32 v50, v197, v50, vcc
	v_cmp_lt_u32_e32 vcc, s47, v16
	v_add_u32_e32 v16, -2, v2
	s_nop 0
	v_cndmask_b32_e32 v51, v197, v51, vcc
	v_cmp_gt_u32_e32 vcc, s71, v16
	v_add_u32_e32 v16, -3, v2
	s_nop 0
	v_cndmask_b32_e32 v52, v197, v52, vcc
	v_cmp_gt_u32_e32 vcc, s71, v16
	v_add_u32_e32 v16, -8, v2
	s_nop 0
	v_cndmask_b32_e32 v53, v197, v53, vcc
	v_cmp_gt_u32_e32 vcc, s71, v16
	v_add_u32_e32 v16, -9, v2
	s_nop 0
	v_cndmask_b32_e32 v54, v197, v54, vcc
	v_cmp_gt_u32_e32 vcc, s71, v16
	v_add_u32_e32 v16, -10, v2
	s_nop 0
	v_cndmask_b32_e32 v55, v197, v55, vcc
	v_cmp_gt_u32_e32 vcc, s71, v16
	v_add_u32_e32 v16, -11, v2
	s_nop 0
	v_cndmask_b32_e32 v56, v197, v56, vcc
	v_cmp_gt_u32_e32 vcc, s71, v16
	v_add_u32_e32 v16, -16, v2
	s_nop 0
	v_cndmask_b32_e32 v57, v197, v57, vcc
	v_cmp_gt_u32_e32 vcc, s71, v16
	v_subrev_u32_e32 v16, 17, v2
	s_nop 0
	v_cndmask_b32_e32 v58, v197, v58, vcc
	v_cmp_gt_u32_e32 vcc, s71, v16
	v_subrev_u32_e32 v16, 18, v2
	s_nop 0
	v_cndmask_b32_e32 v59, v197, v59, vcc
	v_cmp_gt_u32_e32 vcc, s71, v16
	v_subrev_u32_e32 v16, 19, v2
	s_nop 0
	v_cndmask_b32_e32 v60, v197, v60, vcc
	v_cmp_gt_u32_e32 vcc, s71, v16
	v_subrev_u32_e32 v16, 24, v2
	s_nop 0
	v_cndmask_b32_e32 v61, v197, v61, vcc
	v_cmp_gt_u32_e32 vcc, s71, v16
	v_subrev_u32_e32 v16, 25, v2
	s_nop 0
	v_cndmask_b32_e32 v62, v197, v62, vcc
	v_cmp_gt_u32_e32 vcc, s71, v16
	v_subrev_u32_e32 v16, 26, v2
	v_subrev_u32_e32 v2, 27, v2
	v_cndmask_b32_e32 v63, v197, v63, vcc
	v_cmp_gt_u32_e32 vcc, s71, v16
	s_nop 1
	v_cndmask_b32_e32 v64, v197, v64, vcc
	v_cmp_gt_u32_e32 vcc, s71, v2
	s_nop 1
	v_cndmask_b32_e32 v65, v197, v65, vcc

.Lkpre_skip_s:
	ds_read_b128 v[188:191], v118
	ds_read_b128 v[192:195], v117
	ds_read_b128 v[202:205], v116
	s_branch .LBB0_788
